# stack4_reorder
# speedup vs baseline: 1.0204x; 1.0204x over previous
.LBB2_2:
	s_or_b64 exec, exec, s[12:13]
	v_lshrrev_b32_e32 v68, 7, v0
	s_lshl_b32 s0, s2, 4
	v_lshl_or_b32 v34, v68, 2, s0
	v_lshrrev_b32_e32 v2, 1, v0
	v_ashrrev_i32_e32 v35, 31, v34
	v_and_b32_e32 v69, 32, v2
	v_lshlrev_b64 v[2:3], 8, v[34:35]
	v_lshl_add_u64 v[2:3], s[4:5], 0, v[2:3]
	v_lshlrev_b32_e32 v66, 2, v69
	v_lshl_add_u64 v[2:3], v[2:3], 0, v[66:67]
	v_lshlrev_b32_e32 v36, 2, v1
	v_mov_b32_e32 v37, v67
	v_lshl_add_u64 v[2:3], v[2:3], 0, v[36:37]
	v_lshlrev_b32_e32 v38, 22, v72
	v_mov_b32_e32 v39, v67
	v_lshl_add_u64 v[4:5], v[2:3], 0, v[38:39]
	v_or_b32_e32 v40, 0x800000, v38
	v_mov_b32_e32 v41, v67
	global_load_dword v6, v[4:5], off
	v_lshl_add_u64 v[4:5], v[2:3], 0, v[40:41]
	v_or_b32_e32 v42, 0x1000000, v38
	v_mov_b32_e32 v43, v67
	global_load_dword v18, v[4:5], off
	v_lshl_add_u64 v[4:5], v[2:3], 0, v[42:43]
	v_or_b32_e32 v44, 0x1800000, v38
	v_mov_b32_e32 v45, v67
	global_load_dword v19, v[4:5], off
	v_lshl_add_u64 v[4:5], v[2:3], 0, v[44:45]
	v_or_b32_e32 v46, 0x2000000, v38
	v_mov_b32_e32 v47, v67
	global_load_dword v20, v[4:5], off
	v_lshl_add_u64 v[4:5], v[2:3], 0, v[46:47]
	v_or_b32_e32 v48, 0x2800000, v38
	v_mov_b32_e32 v49, v67
	global_load_dword v21, v[4:5], off
	v_lshl_add_u64 v[4:5], v[2:3], 0, v[48:49]
	v_or_b32_e32 v50, 0x3000000, v38
	v_mov_b32_e32 v51, v67
	global_load_dword v22, v[4:5], off
	v_lshl_add_u64 v[4:5], v[2:3], 0, v[50:51]
	v_or_b32_e32 v52, 0x3800000, v38
	v_mov_b32_e32 v53, v67
	global_load_dword v23, v[4:5], off
	v_lshl_add_u64 v[4:5], v[2:3], 0, v[52:53]
	v_or_b32_e32 v54, 0x4000000, v38
	v_mov_b32_e32 v55, v67
	global_load_dword v24, v[4:5], off
	v_lshl_add_u64 v[4:5], v[2:3], 0, v[54:55]
	v_or_b32_e32 v56, 0x4800000, v38
	v_mov_b32_e32 v57, v67
	global_load_dword v25, v[4:5], off
	v_lshl_add_u64 v[4:5], v[2:3], 0, v[56:57]
	v_or_b32_e32 v58, 0x5000000, v38
	v_mov_b32_e32 v59, v67
	global_load_dword v26, v[4:5], off
	v_lshl_add_u64 v[4:5], v[2:3], 0, v[58:59]
	v_or_b32_e32 v60, 0x5800000, v38
	v_mov_b32_e32 v61, v67
	s_mov_b64 s[6:7], 0x6000000
	global_load_dword v27, v[4:5], off
	v_lshl_add_u64 v[4:5], v[2:3], 0, v[60:61]
	v_lshl_add_u64 v[2:3], v[2:3], 0, s[6:7]
	global_load_dword v28, v[4:5], off
	global_load_dword v29, v[2:3], off
	v_or_b32_e32 v2, 1, v34
	v_ashrrev_i32_e32 v3, 31, v2
	v_lshlrev_b64 v[2:3], 8, v[2:3]
	v_lshl_add_u64 v[2:3], s[4:5], 0, v[2:3]
	v_lshl_add_u64 v[2:3], v[2:3], 0, v[66:67]
	v_lshl_add_u64 v[2:3], v[2:3], 0, v[36:37]
	v_lshl_add_u64 v[4:5], v[2:3], 0, v[38:39]
	global_load_dword v30, v[4:5], off
	v_lshl_add_u64 v[4:5], v[2:3], 0, v[40:41]
	global_load_dword v35, v[4:5], off
	v_lshl_add_u64 v[4:5], v[2:3], 0, v[42:43]
	global_load_dword v63, v[4:5], off
	v_lshl_add_u64 v[4:5], v[2:3], 0, v[44:45]
	global_load_dword v64, v[4:5], off
	v_lshl_add_u64 v[4:5], v[2:3], 0, v[46:47]
	global_load_dword v65, v[4:5], off
	v_lshl_add_u64 v[4:5], v[2:3], 0, v[48:49]
	global_load_dword v83, v[4:5], off
	v_lshl_add_u64 v[4:5], v[2:3], 0, v[50:51]
	global_load_dword v84, v[4:5], off
	v_lshl_add_u64 v[4:5], v[2:3], 0, v[52:53]
	global_load_dword v85, v[4:5], off
	v_lshl_add_u64 v[4:5], v[2:3], 0, v[54:55]
	global_load_dword v86, v[4:5], off
	v_lshl_add_u64 v[4:5], v[2:3], 0, v[56:57]
	global_load_dword v87, v[4:5], off
	v_lshl_add_u64 v[4:5], v[2:3], 0, v[58:59]
	global_load_dword v88, v[4:5], off
	v_lshl_add_u64 v[4:5], v[2:3], 0, v[60:61]
	global_load_dword v89, v[4:5], off
	v_lshl_add_u64 v[2:3], v[2:3], 0, s[6:7]
	global_load_dword v90, v[2:3], off
	s_waitcnt vmcnt(13)
	s_mov_b32 s0, 0xff61b1e6
	v_mfma_f32_32x32x2_f32 v[2:17], v62, v6, 0
	v_or_b32_e32 v1, v69, v1
	v_lshlrev_b32_e32 v1, 9, v1
	v_mfma_f32_32x32x2_f32 v[2:17], v82, v18, v[2:17]
	v_or_b32_e32 v18, 2, v34
	v_or_b32_e32 v34, 3, v34
	v_mfma_f32_32x32x2_f32 v[2:17], v81, v19, v[2:17]
	v_ashrrev_i32_e32 v19, 31, v18
	v_lshlrev_b64 v[18:19], 8, v[18:19]
	v_lshl_add_u64 v[18:19], s[4:5], 0, v[18:19]
	v_lshl_add_u64 v[18:19], v[18:19], 0, v[66:67]
	v_lshl_add_u64 v[18:19], v[18:19], 0, v[36:37]
	v_mfma_f32_32x32x2_f32 v[2:17], v80, v20, v[2:17]
	v_mfma_f32_32x32x2_f32 v[2:17], v79, v21, v[2:17]
	v_lshl_add_u64 v[20:21], v[18:19], 0, v[38:39]
	global_load_dword v91, v[20:21], off
	v_lshl_add_u64 v[20:21], v[18:19], 0, v[40:41]
	global_load_dword v92, v[20:21], off
	v_lshl_add_u64 v[20:21], v[18:19], 0, v[42:43]
	global_load_dword v93, v[20:21], off
	v_lshl_add_u64 v[20:21], v[18:19], 0, v[44:45]
	global_load_dword v94, v[20:21], off
	v_lshl_add_u64 v[20:21], v[18:19], 0, v[46:47]
	global_load_dword v95, v[20:21], off
	v_lshl_add_u64 v[20:21], v[18:19], 0, v[48:49]
	global_load_dword v96, v[20:21], off
	v_lshl_add_u64 v[20:21], v[18:19], 0, v[50:51]
	global_load_dword v97, v[20:21], off
	v_lshl_add_u64 v[20:21], v[18:19], 0, v[52:53]
	v_mfma_f32_32x32x2_f32 v[2:17], v78, v22, v[2:17]
	global_load_dword v98, v[20:21], off
	v_lshl_add_u64 v[20:21], v[18:19], 0, v[54:55]
	global_load_dword v99, v[20:21], off
	v_lshl_add_u64 v[20:21], v[18:19], 0, v[56:57]
	global_load_dword v100, v[20:21], off
	v_lshl_add_u64 v[20:21], v[18:19], 0, v[58:59]
	global_load_dword v101, v[20:21], off
	v_lshl_add_u64 v[20:21], v[18:19], 0, v[60:61]
	global_load_dword v102, v[20:21], off
	v_lshl_add_u64 v[18:19], v[18:19], 0, s[6:7]
	global_load_dword v103, v[18:19], off
	s_waitcnt vmcnt(13)
	v_mfma_f32_32x32x2_f32 v[2:17], v77, v23, v[2:17]
	v_mfma_f32_32x32x2_f32 v[2:17], v76, v24, v[2:17]
	v_mfma_f32_32x32x2_f32 v[2:17], v75, v25, v[2:17]
	v_mfma_f32_32x32x2_f32 v[2:17], v74, v26, v[2:17]
	v_mfma_f32_32x32x2_f32 v[2:17], v73, v27, v[2:17]
	v_mfma_f32_32x32x2_f32 v[2:17], v71, v28, v[2:17]
	v_mfma_f32_32x32x2_f32 v[2:17], v70, v29, v[2:17]
	v_mfma_f32_32x32x2_f32 v[18:33], v62, v30, 0
	v_mfma_f32_32x32x2_f32 v[18:33], v82, v35, v[18:33]
	v_ashrrev_i32_e32 v35, 31, v34
	v_lshlrev_b64 v[34:35], 8, v[34:35]
	v_lshl_add_u64 v[34:35], s[4:5], 0, v[34:35]
	v_lshl_add_u64 v[34:35], v[34:35], 0, v[66:67]
	v_lshl_add_u64 v[34:35], v[34:35], 0, v[36:37]
	v_lshl_add_u64 v[36:37], v[34:35], 0, v[38:39]
	v_mfma_f32_32x32x2_f32 v[18:33], v81, v63, v[18:33]
	global_load_dword v63, v[36:37], off
	v_lshl_add_u64 v[36:37], v[34:35], 0, v[40:41]
	global_load_dword v66, v[36:37], off
	v_lshl_add_u64 v[36:37], v[34:35], 0, v[42:43]
	v_mfma_f32_32x32x2_f32 v[18:33], v80, v64, v[18:33]
	v_mfma_f32_32x32x2_f32 v[18:33], v79, v65, v[18:33]
	v_mfma_f32_32x32x2_f32 v[18:33], v78, v83, v[18:33]
	global_load_dword v83, v[36:37], off
	v_lshl_add_u64 v[36:37], v[34:35], 0, v[44:45]
	v_mfma_f32_32x32x2_f32 v[18:33], v77, v84, v[18:33]
	global_load_dword v84, v[36:37], off
	v_lshl_add_u64 v[36:37], v[34:35], 0, v[46:47]
	v_mfma_f32_32x32x2_f32 v[18:33], v76, v85, v[18:33]
	global_load_dword v85, v[36:37], off
	v_lshl_add_u64 v[36:37], v[34:35], 0, v[48:49]
	v_mfma_f32_32x32x2_f32 v[18:33], v75, v86, v[18:33]
	global_load_dword v86, v[36:37], off
	v_lshl_add_u64 v[36:37], v[34:35], 0, v[50:51]
	v_mfma_f32_32x32x2_f32 v[18:33], v74, v87, v[18:33]
	global_load_dword v87, v[36:37], off
	v_lshl_add_u64 v[36:37], v[34:35], 0, v[52:53]
	v_mfma_f32_32x32x2_f32 v[18:33], v73, v88, v[18:33]
	global_load_dword v88, v[36:37], off
	v_lshl_add_u64 v[36:37], v[34:35], 0, v[54:55]
	v_mfma_f32_32x32x2_f32 v[18:33], v71, v89, v[18:33]
	global_load_dword v89, v[36:37], off
	v_lshl_add_u64 v[36:37], v[34:35], 0, v[56:57]
	v_mfma_f32_32x32x2_f32 v[18:33], v70, v90, v[18:33]
	global_load_dword v90, v[36:37], off
	v_lshl_add_u64 v[36:37], v[34:35], 0, v[58:59]
	global_load_dword v104, v[36:37], off
	v_lshl_add_u64 v[36:37], v[34:35], 0, v[60:61]
	global_load_dword v105, v[36:37], off
	v_lshl_add_u64 v[34:35], v[34:35], 0, s[6:7]
	global_load_dword v106, v[34:35], off
	s_waitcnt vmcnt(13)
	s_nop 14
	v_max3_f32 v2, v2, s0, v18
	s_waitcnt vmcnt(0)
	v_mfma_f32_32x32x2_f32 v[34:49], v62, v91, 0
	v_max3_f32 v3, v3, s0, v19
	v_max3_f32 v4, v4, s0, v20
	v_max3_f32 v5, v5, s0, v21
	v_max3_f32 v6, v6, s0, v22
	v_max3_f32 v7, v7, s0, v23
	v_max3_f32 v8, v8, s0, v24
	v_max3_f32 v9, v9, s0, v25
	v_lshlrev_b32_e32 v18, 5, v68
	v_max3_f32 v10, v10, s0, v26
	v_max3_f32 v11, v11, s0, v27
	v_max3_f32 v12, v12, s0, v28
	v_max3_f32 v13, v13, s0, v29
	v_max3_f32 v14, v14, s0, v30
	v_max3_f32 v15, v15, s0, v31
	v_max3_f32 v16, v16, s0, v32
	v_mfma_f32_32x32x2_f32 v[50:65], v62, v63, 0
	v_max3_f32 v17, v17, s0, v33
	s_lshl_b32 s0, s2, 2
	s_mov_b32 s2, 0x7f000
	v_mfma_f32_32x32x2_f32 v[34:49], v82, v92, v[34:49]
	v_mfma_f32_32x32x2_f32 v[50:65], v82, v66, v[50:65]
	v_lshlrev_b32_e32 v66, 4, v72
	v_or3_b32 v1, v1, v18, v66
	v_mfma_f32_32x32x2_f32 v[34:49], v81, v93, v[34:49]
	v_mfma_f32_32x32x2_f32 v[50:65], v81, v83, v[50:65]
	v_mfma_f32_32x32x2_f32 v[34:49], v80, v94, v[34:49]
	v_mfma_f32_32x32x2_f32 v[50:65], v80, v84, v[50:65]
	v_mfma_f32_32x32x2_f32 v[34:49], v79, v95, v[34:49]
	v_mfma_f32_32x32x2_f32 v[50:65], v79, v85, v[50:65]
	v_mfma_f32_32x32x2_f32 v[34:49], v78, v96, v[34:49]
	v_mfma_f32_32x32x2_f32 v[50:65], v78, v86, v[50:65]
	v_mfma_f32_32x32x2_f32 v[34:49], v77, v97, v[34:49]
	v_mfma_f32_32x32x2_f32 v[50:65], v77, v87, v[50:65]
	v_mfma_f32_32x32x2_f32 v[34:49], v76, v98, v[34:49]
	v_mfma_f32_32x32x2_f32 v[50:65], v76, v88, v[50:65]
	v_mfma_f32_32x32x2_f32 v[34:49], v75, v99, v[34:49]
	v_mfma_f32_32x32x2_f32 v[50:65], v75, v89, v[50:65]
	v_mfma_f32_32x32x2_f32 v[34:49], v74, v100, v[34:49]
	v_mfma_f32_32x32x2_f32 v[50:65], v74, v90, v[50:65]
	global_load_dwordx4 v[74:77], v66, s[8:9]
	global_load_dwordx4 v[78:81], v66, s[8:9] offset:32
	global_load_dwordx4 v[82:85], v66, s[8:9] offset:64
	global_load_dwordx4 v[86:89], v66, s[8:9] offset:96
	v_mfma_f32_32x32x2_f32 v[34:49], v73, v101, v[34:49]
	v_mfma_f32_32x32x2_f32 v[50:65], v73, v104, v[50:65]
	v_mfma_f32_32x32x2_f32 v[34:49], v71, v102, v[34:49]
	v_mfma_f32_32x32x2_f32 v[50:65], v71, v105, v[50:65]
	v_mfma_f32_32x32x2_f32 v[34:49], v70, v103, v[34:49]
	v_mfma_f32_32x32x2_f32 v[50:65], v70, v106, v[50:65]
	s_nop 15
	s_nop 1
	v_max3_f32 v2, v2, v34, v50
	v_max3_f32 v3, v3, v35, v51
	v_max3_f32 v4, v4, v36, v52
	v_max3_f32 v5, v5, v37, v53
	s_waitcnt vmcnt(3)
	v_add_f32_e32 v2, v2, v74
	v_add_f32_e32 v3, v3, v75
	v_add_f32_e32 v4, v4, v76
	v_add_f32_e32 v5, v5, v77
	v_max3_f32 v6, v6, v38, v54
	v_max3_f32 v7, v7, v39, v55
	v_max3_f32 v8, v8, v40, v56
	v_max3_f32 v9, v9, v41, v57
	v_max_f32_e32 v2, 0, v2
	v_max_f32_e32 v3, 0, v3
	v_max_f32_e32 v4, 0, v4
	v_max_f32_e32 v5, 0, v5
	ds_write_b128 v1, v[2:5]
	s_waitcnt vmcnt(2)
	v_add_f32_e32 v2, v6, v78
	v_add_f32_e32 v3, v7, v79
	v_add_f32_e32 v4, v8, v80
	v_add_f32_e32 v5, v9, v81
	v_max3_f32 v10, v10, v42, v58
	v_max3_f32 v11, v11, v43, v59
	v_max3_f32 v12, v12, v44, v60
	v_max3_f32 v13, v13, v45, v61
	v_max_f32_e32 v2, 0, v2
	v_max_f32_e32 v3, 0, v3
	v_max_f32_e32 v4, 0, v4
	v_max_f32_e32 v5, 0, v5
	ds_write_b128 v1, v[2:5] offset:128
	s_waitcnt vmcnt(1)
	v_add_f32_e32 v2, v10, v82
	v_add_f32_e32 v3, v11, v83
	v_add_f32_e32 v4, v12, v84
	v_add_f32_e32 v5, v13, v85
	v_max3_f32 v14, v14, v46, v62
	v_max3_f32 v15, v15, v47, v63
	v_max3_f32 v16, v16, v48, v64
	v_max3_f32 v17, v17, v49, v65
	v_max_f32_e32 v2, 0, v2
	v_max_f32_e32 v3, 0, v3
	v_max_f32_e32 v4, 0, v4
	v_max_f32_e32 v5, 0, v5
	ds_write_b128 v1, v[2:5] offset:256
	s_waitcnt vmcnt(0)
	v_add_f32_e32 v2, v14, v86
	v_add_f32_e32 v3, v15, v87
	v_add_f32_e32 v4, v16, v88
	v_add_f32_e32 v5, v17, v89
	v_max_f32_e32 v2, 0, v2
	v_max_f32_e32 v3, 0, v3
	v_max_f32_e32 v4, 0, v4
	v_max_f32_e32 v5, 0, v5
	v_lshlrev_b32_e32 v12, 4, v0
	ds_write_b128 v1, v[2:5] offset:384
	s_waitcnt lgkmcnt(0)
	s_barrier
	v_and_b32_e32 v66, 0x70, v12
	v_lshlrev_b32_e32 v13, 9, v0
	ds_read_b128 v[0:3], v12
	v_lshl_add_u64 v[8:9], s[10:11], 0, v[66:67]
	v_and_b32_e32 v66, 0x3f000, v13
	v_lshl_add_u64 v[4:5], v[66:67], 0, s[0:1]
	v_lshlrev_b64 v[4:5], 5, v[4:5]
	v_lshl_add_u64 v[10:11], v[8:9], 0, v[4:5]
	ds_read_b128 v[4:7], v12 offset:8192
	s_waitcnt lgkmcnt(1)
	global_store_dwordx4 v[10:11], v[0:3], off sc1
	s_nop 1
	v_mov_b32_e32 v0, 0x40000
	v_bitop3_b32 v66, v13, s2, v0 bitop3:0xc8
	v_lshl_add_u64 v[0:1], v[66:67], 0, s[0:1]
	v_lshlrev_b64 v[0:1], 5, v[0:1]
	v_lshl_add_u64 v[0:1], v[8:9], 0, v[0:1]
	s_waitcnt lgkmcnt(0)
	global_store_dwordx4 v[0:1], v[4:7], off sc1
	s_mov_b32 s2, 0xbf000
	v_mov_b32_e32 v0, 0x80000
	v_bitop3_b32 v66, v13, s2, v0 bitop3:0xc8
	ds_read_b128 v[0:3], v12 offset:16384
	v_lshl_add_u64 v[4:5], v[66:67], 0, s[0:1]
	v_lshlrev_b64 v[4:5], 5, v[4:5]
	v_lshl_add_u64 v[10:11], v[8:9], 0, v[4:5]
	ds_read_b128 v[4:7], v12 offset:24576
	s_waitcnt lgkmcnt(1)
	global_store_dwordx4 v[10:11], v[0:3], off sc1
	s_mov_b32 s2, 0xff000
	s_nop 0
	v_mov_b32_e32 v0, 0xc0000
	v_bitop3_b32 v66, v13, s2, v0 bitop3:0xc8
	v_lshl_add_u64 v[0:1], v[66:67], 0, s[0:1]
	v_lshlrev_b64 v[0:1], 5, v[0:1]
	v_lshl_add_u64 v[0:1], v[8:9], 0, v[0:1]
	s_waitcnt lgkmcnt(0)
	global_store_dwordx4 v[0:1], v[4:7], off sc1
	s_barrier
	s_lshr_b32 s2, s0, 2
	s_cmp_gt_u32 s2, 63
	s_cbranch_scc1 .Lro_done
	v_lshrrev_b32_e32 v0, 4, v12
	v_cmp_gt_u32_e32 vcc, 64, v0
	s_and_saveexec_b64 s[4:5], vcc
	s_cbranch_execz .Lro_done
	s_lshl_b32 s3, s2, 2
	s_add_u32 s6, s10, 0x2050600
	s_addc_u32 s7, s11, 0
	s_add_u32 s6, s6, s3
	s_addc_u32 s7, s7, 0
	s_load_dword s14, s[6:7], 0x0
	s_load_dword s15, s[6:7], 0x100
	s_add_u32 s16, s10, 0x2050900
	s_addc_u32 s17, s11, 0
	v_and_b32_e32 v2, 15, v0
	v_mov_b32_e32 v11, 0
	s_mov_b32 s35, 0x10001
	v_cmp_lt_u32_e32 vcc, 3, v2
	s_nop 1
	v_cndmask_b32_e64 v30, 0, 8, vcc
	v_cmp_lt_u32_e32 vcc, 7, v2
	v_mov_b32_e32 v29, 12
	s_nop 0
	v_cndmask_b32_e32 v30, v30, v29, vcc
	v_cndmask_b32_e64 v31, 4, 8, vcc
	v_cmp_lt_u32_e32 vcc, 11, v2
	v_and_b32_e32 v28, 16, v0
	s_nop 0
	v_cndmask_b32_e64 v31, v31, 16, vcc
	v_cmp_ne_u32_e32 vcc, 0, v28
	v_and_b32_e32 v1, 32, v0
	s_nop 0
	v_cndmask_b32_e32 v30, v30, v31, vcc
	v_add3_u32 v1, v1, v2, v30
	v_lshlrev_b32_e32 v8, 3, v0
	v_lshlrev_b32_e32 v9, 2, v0
	v_add_u32_e32 v9, 0x2000, v9
	v_lshlrev_b32_e32 v10, 4, v1
	v_mov_b32_e32 v24, 0
	v_mov_b32_e32 v25, 0
	ds_write_b64 v8, v[24:25] offset:0
	ds_write_b64 v8, v[24:25] offset:512
	ds_write_b64 v8, v[24:25] offset:1024
	ds_write_b64 v8, v[24:25] offset:1536
	ds_write_b64 v8, v[24:25] offset:2048
	ds_write_b64 v8, v[24:25] offset:2560
	ds_write_b64 v8, v[24:25] offset:3072
	ds_write_b64 v8, v[24:25] offset:3584
	ds_write_b64 v8, v[24:25] offset:4096
	ds_write_b64 v8, v[24:25] offset:4608
	ds_write_b64 v8, v[24:25] offset:5120
	ds_write_b64 v8, v[24:25] offset:5632
	ds_write_b64 v8, v[24:25] offset:6144
	ds_write_b64 v8, v[24:25] offset:6656
	ds_write_b64 v8, v[24:25] offset:7168
	ds_write_b64 v8, v[24:25] offset:7680
	v_mov_b32_e32 v7, 0
	v_mov_b32_e32 v6, 0
	s_waitcnt lgkmcnt(0)
	s_cmp_eq_u32 s14, 0
	s_cbranch_scc1 .Lro_done
	s_cmp_gt_u32 s14, 64
	s_cbranch_scc1 .Lro_done
	s_lshl_b32 s15, s15, 2
	s_add_u32 s16, s16, s15
	s_addc_u32 s17, s17, 0
	s_mov_b64 s[18:19], s[16:17]
	s_cmp_le_u32 s14, 0
	s_cbranch_scc1 .Lro_loaded
	global_load_dwordx4 v[32:35], v10, s[18:19]
	s_add_u32 s18, s18, 0x400
	s_addc_u32 s19, s19, 0
	s_cmp_le_u32 s14, 4
	s_cbranch_scc1 .Lro_loaded
	global_load_dwordx4 v[36:39], v10, s[18:19]
	s_add_u32 s18, s18, 0x400
	s_addc_u32 s19, s19, 0
	s_cmp_le_u32 s14, 8
	s_cbranch_scc1 .Lro_loaded
	global_load_dwordx4 v[40:43], v10, s[18:19]
	s_add_u32 s18, s18, 0x400
	s_addc_u32 s19, s19, 0
	s_cmp_le_u32 s14, 12
	s_cbranch_scc1 .Lro_loaded
	global_load_dwordx4 v[44:47], v10, s[18:19]
	s_add_u32 s18, s18, 0x400
	s_addc_u32 s19, s19, 0
	s_cmp_le_u32 s14, 16
	s_cbranch_scc1 .Lro_loaded
	global_load_dwordx4 v[48:51], v10, s[18:19]
	s_add_u32 s18, s18, 0x400
	s_addc_u32 s19, s19, 0
	s_cmp_le_u32 s14, 20
	s_cbranch_scc1 .Lro_loaded
	global_load_dwordx4 v[52:55], v10, s[18:19]
	s_add_u32 s18, s18, 0x400
	s_addc_u32 s19, s19, 0
	s_cmp_le_u32 s14, 24
	s_cbranch_scc1 .Lro_loaded
	global_load_dwordx4 v[56:59], v10, s[18:19]
	s_add_u32 s18, s18, 0x400
	s_addc_u32 s19, s19, 0
	s_cmp_le_u32 s14, 28
	s_cbranch_scc1 .Lro_loaded
	global_load_dwordx4 v[60:63], v10, s[18:19]
	s_add_u32 s18, s18, 0x400
	s_addc_u32 s19, s19, 0
	s_cmp_le_u32 s14, 32
	s_cbranch_scc1 .Lro_loaded
	global_load_dwordx4 v[64:67], v10, s[18:19]
	s_add_u32 s18, s18, 0x400
	s_addc_u32 s19, s19, 0
	s_cmp_le_u32 s14, 36
	s_cbranch_scc1 .Lro_loaded
	global_load_dwordx4 v[68:71], v10, s[18:19]
	s_add_u32 s18, s18, 0x400
	s_addc_u32 s19, s19, 0
	s_cmp_le_u32 s14, 40
	s_cbranch_scc1 .Lro_loaded
	global_load_dwordx4 v[72:75], v10, s[18:19]
	s_add_u32 s18, s18, 0x400
	s_addc_u32 s19, s19, 0
	s_cmp_le_u32 s14, 44
	s_cbranch_scc1 .Lro_loaded
	global_load_dwordx4 v[76:79], v10, s[18:19]
	s_add_u32 s18, s18, 0x400
	s_addc_u32 s19, s19, 0
	s_cmp_le_u32 s14, 48
	s_cbranch_scc1 .Lro_loaded
	global_load_dwordx4 v[80:83], v10, s[18:19]
	s_add_u32 s18, s18, 0x400
	s_addc_u32 s19, s19, 0
	s_cmp_le_u32 s14, 52
	s_cbranch_scc1 .Lro_loaded
	global_load_dwordx4 v[84:87], v10, s[18:19]
	s_add_u32 s18, s18, 0x400
	s_addc_u32 s19, s19, 0
	s_cmp_le_u32 s14, 56
	s_cbranch_scc1 .Lro_loaded
	global_load_dwordx4 v[88:91], v10, s[18:19]
	s_add_u32 s18, s18, 0x400
	s_addc_u32 s19, s19, 0
	s_cmp_le_u32 s14, 60
	s_cbranch_scc1 .Lro_loaded
	global_load_dwordx4 v[92:95], v10, s[18:19]
	s_add_u32 s18, s18, 0x400
	s_addc_u32 s19, s19, 0
.Lro_loaded:
	s_waitcnt vmcnt(0)
	s_mov_b32 s36, 0xffff
	s_cmp_le_u32 s14, 0
	s_cbranch_scc1 .Lro_built
	v_cmp_lt_u32_e32 vcc, s36, v32
	s_mov_b64 exec, vcc
	ds_write_b32 v9, v32 offset:0
	v_bfe_u32 v27, v32, 4, 4
	v_add_u32_e32 v6, 1, v6
	v_lshlrev_b32_e64 v28, v27, s35
	v_or_b32_e32 v7, v7, v28
	v_lshl_add_u32 v27, v27, 9, v8
	v_mov_b32_e32 v24, 1
	v_mov_b32_e32 v25, 0
	ds_or_b64 v27, v[24:25]
	s_mov_b64 exec, -1
	v_cmp_lt_u32_e32 vcc, s36, v33
	s_mov_b64 exec, vcc
	ds_write_b32 v9, v33 offset:256
	v_bfe_u32 v27, v33, 4, 4
	v_add_u32_e32 v6, 1, v6
	v_lshlrev_b32_e64 v28, v27, s35
	v_or_b32_e32 v7, v7, v28
	v_lshl_add_u32 v27, v27, 9, v8
	v_mov_b32_e32 v24, 2
	v_mov_b32_e32 v25, 0
	ds_or_b64 v27, v[24:25]
	s_mov_b64 exec, -1
	v_cmp_lt_u32_e32 vcc, s36, v34
	s_mov_b64 exec, vcc
	ds_write_b32 v9, v34 offset:512
	v_bfe_u32 v27, v34, 4, 4
	v_add_u32_e32 v6, 1, v6
	v_lshlrev_b32_e64 v28, v27, s35
	v_or_b32_e32 v7, v7, v28
	v_lshl_add_u32 v27, v27, 9, v8
	v_mov_b32_e32 v24, 4
	v_mov_b32_e32 v25, 0
	ds_or_b64 v27, v[24:25]
	s_mov_b64 exec, -1
	v_cmp_lt_u32_e32 vcc, s36, v35
	s_mov_b64 exec, vcc
	ds_write_b32 v9, v35 offset:768
	v_bfe_u32 v27, v35, 4, 4
	v_add_u32_e32 v6, 1, v6
	v_lshlrev_b32_e64 v28, v27, s35
	v_or_b32_e32 v7, v7, v28
	v_lshl_add_u32 v27, v27, 9, v8
	v_mov_b32_e32 v24, 8
	v_mov_b32_e32 v25, 0
	ds_or_b64 v27, v[24:25]
	s_mov_b64 exec, -1
	s_cmp_le_u32 s14, 4
	s_cbranch_scc1 .Lro_built
	v_cmp_lt_u32_e32 vcc, s36, v36
	s_mov_b64 exec, vcc
	ds_write_b32 v9, v36 offset:1024
	v_bfe_u32 v27, v36, 4, 4
	v_add_u32_e32 v6, 1, v6
	v_lshlrev_b32_e64 v28, v27, s35
	v_or_b32_e32 v7, v7, v28
	v_lshl_add_u32 v27, v27, 9, v8
	v_mov_b32_e32 v24, 16
	v_mov_b32_e32 v25, 0
	ds_or_b64 v27, v[24:25]
	s_mov_b64 exec, -1
	v_cmp_lt_u32_e32 vcc, s36, v37
	s_mov_b64 exec, vcc
	ds_write_b32 v9, v37 offset:1280
	v_bfe_u32 v27, v37, 4, 4
	v_add_u32_e32 v6, 1, v6
	v_lshlrev_b32_e64 v28, v27, s35
	v_or_b32_e32 v7, v7, v28
	v_lshl_add_u32 v27, v27, 9, v8
	v_mov_b32_e32 v24, 32
	v_mov_b32_e32 v25, 0
	ds_or_b64 v27, v[24:25]
	s_mov_b64 exec, -1
	v_cmp_lt_u32_e32 vcc, s36, v38
	s_mov_b64 exec, vcc
	ds_write_b32 v9, v38 offset:1536
	v_bfe_u32 v27, v38, 4, 4
	v_add_u32_e32 v6, 1, v6
	v_lshlrev_b32_e64 v28, v27, s35
	v_or_b32_e32 v7, v7, v28
	v_lshl_add_u32 v27, v27, 9, v8
	v_mov_b32_e32 v24, 64
	v_mov_b32_e32 v25, 0
	ds_or_b64 v27, v[24:25]
	s_mov_b64 exec, -1
	v_cmp_lt_u32_e32 vcc, s36, v39
	s_mov_b64 exec, vcc
	ds_write_b32 v9, v39 offset:1792
	v_bfe_u32 v27, v39, 4, 4
	v_add_u32_e32 v6, 1, v6
	v_lshlrev_b32_e64 v28, v27, s35
	v_or_b32_e32 v7, v7, v28
	v_lshl_add_u32 v27, v27, 9, v8
	v_mov_b32_e32 v24, 0x80
	v_mov_b32_e32 v25, 0
	ds_or_b64 v27, v[24:25]
	s_mov_b64 exec, -1
	s_cmp_le_u32 s14, 8
	s_cbranch_scc1 .Lro_built
	v_cmp_lt_u32_e32 vcc, s36, v40
	s_mov_b64 exec, vcc
	ds_write_b32 v9, v40 offset:2048
	v_bfe_u32 v27, v40, 4, 4
	v_add_u32_e32 v6, 1, v6
	v_lshlrev_b32_e64 v28, v27, s35
	v_or_b32_e32 v7, v7, v28
	v_lshl_add_u32 v27, v27, 9, v8
	v_mov_b32_e32 v24, 0x100
	v_mov_b32_e32 v25, 0
	ds_or_b64 v27, v[24:25]
	s_mov_b64 exec, -1
	v_cmp_lt_u32_e32 vcc, s36, v41
	s_mov_b64 exec, vcc
	ds_write_b32 v9, v41 offset:2304
	v_bfe_u32 v27, v41, 4, 4
	v_add_u32_e32 v6, 1, v6
	v_lshlrev_b32_e64 v28, v27, s35
	v_or_b32_e32 v7, v7, v28
	v_lshl_add_u32 v27, v27, 9, v8
	v_mov_b32_e32 v24, 0x200
	v_mov_b32_e32 v25, 0
	ds_or_b64 v27, v[24:25]
	s_mov_b64 exec, -1
	v_cmp_lt_u32_e32 vcc, s36, v42
	s_mov_b64 exec, vcc
	ds_write_b32 v9, v42 offset:2560
	v_bfe_u32 v27, v42, 4, 4
	v_add_u32_e32 v6, 1, v6
	v_lshlrev_b32_e64 v28, v27, s35
	v_or_b32_e32 v7, v7, v28
	v_lshl_add_u32 v27, v27, 9, v8
	v_mov_b32_e32 v24, 0x400
	v_mov_b32_e32 v25, 0
	ds_or_b64 v27, v[24:25]
	s_mov_b64 exec, -1
	v_cmp_lt_u32_e32 vcc, s36, v43
	s_mov_b64 exec, vcc
	ds_write_b32 v9, v43 offset:2816
	v_bfe_u32 v27, v43, 4, 4
	v_add_u32_e32 v6, 1, v6
	v_lshlrev_b32_e64 v28, v27, s35
	v_or_b32_e32 v7, v7, v28
	v_lshl_add_u32 v27, v27, 9, v8
	v_mov_b32_e32 v24, 0x800
	v_mov_b32_e32 v25, 0
	ds_or_b64 v27, v[24:25]
	s_mov_b64 exec, -1
	s_cmp_le_u32 s14, 12
	s_cbranch_scc1 .Lro_built
	v_cmp_lt_u32_e32 vcc, s36, v44
	s_mov_b64 exec, vcc
	ds_write_b32 v9, v44 offset:3072
	v_bfe_u32 v27, v44, 4, 4
	v_add_u32_e32 v6, 1, v6
	v_lshlrev_b32_e64 v28, v27, s35
	v_or_b32_e32 v7, v7, v28
	v_lshl_add_u32 v27, v27, 9, v8
	v_mov_b32_e32 v24, 0x1000
	v_mov_b32_e32 v25, 0
	ds_or_b64 v27, v[24:25]
	s_mov_b64 exec, -1
	v_cmp_lt_u32_e32 vcc, s36, v45
	s_mov_b64 exec, vcc
	ds_write_b32 v9, v45 offset:3328
	v_bfe_u32 v27, v45, 4, 4
	v_add_u32_e32 v6, 1, v6
	v_lshlrev_b32_e64 v28, v27, s35
	v_or_b32_e32 v7, v7, v28
	v_lshl_add_u32 v27, v27, 9, v8
	v_mov_b32_e32 v24, 0x2000
	v_mov_b32_e32 v25, 0
	ds_or_b64 v27, v[24:25]
	s_mov_b64 exec, -1
	v_cmp_lt_u32_e32 vcc, s36, v46
	s_mov_b64 exec, vcc
	ds_write_b32 v9, v46 offset:3584
	v_bfe_u32 v27, v46, 4, 4
	v_add_u32_e32 v6, 1, v6
	v_lshlrev_b32_e64 v28, v27, s35
	v_or_b32_e32 v7, v7, v28
	v_lshl_add_u32 v27, v27, 9, v8
	v_mov_b32_e32 v24, 0x4000
	v_mov_b32_e32 v25, 0
	ds_or_b64 v27, v[24:25]
	s_mov_b64 exec, -1
	v_cmp_lt_u32_e32 vcc, s36, v47
	s_mov_b64 exec, vcc
	ds_write_b32 v9, v47 offset:3840
	v_bfe_u32 v27, v47, 4, 4
	v_add_u32_e32 v6, 1, v6
	v_lshlrev_b32_e64 v28, v27, s35
	v_or_b32_e32 v7, v7, v28
	v_lshl_add_u32 v27, v27, 9, v8
	v_mov_b32_e32 v24, 0x8000
	v_mov_b32_e32 v25, 0
	ds_or_b64 v27, v[24:25]
	s_mov_b64 exec, -1
	s_cmp_le_u32 s14, 16
	s_cbranch_scc1 .Lro_built
	v_cmp_lt_u32_e32 vcc, s36, v48
	s_mov_b64 exec, vcc
	ds_write_b32 v9, v48 offset:4096
	v_bfe_u32 v27, v48, 4, 4
	v_add_u32_e32 v6, 1, v6
	v_lshlrev_b32_e64 v28, v27, s35
	v_or_b32_e32 v7, v7, v28
	v_lshl_add_u32 v27, v27, 9, v8
	v_mov_b32_e32 v24, 0x10000
	v_mov_b32_e32 v25, 0
	ds_or_b64 v27, v[24:25]
	s_mov_b64 exec, -1
	v_cmp_lt_u32_e32 vcc, s36, v49
	s_mov_b64 exec, vcc
	ds_write_b32 v9, v49 offset:4352
	v_bfe_u32 v27, v49, 4, 4
	v_add_u32_e32 v6, 1, v6
	v_lshlrev_b32_e64 v28, v27, s35
	v_or_b32_e32 v7, v7, v28
	v_lshl_add_u32 v27, v27, 9, v8
	v_mov_b32_e32 v24, 0x20000
	v_mov_b32_e32 v25, 0
	ds_or_b64 v27, v[24:25]
	s_mov_b64 exec, -1
	v_cmp_lt_u32_e32 vcc, s36, v50
	s_mov_b64 exec, vcc
	ds_write_b32 v9, v50 offset:4608
	v_bfe_u32 v27, v50, 4, 4
	v_add_u32_e32 v6, 1, v6
	v_lshlrev_b32_e64 v28, v27, s35
	v_or_b32_e32 v7, v7, v28
	v_lshl_add_u32 v27, v27, 9, v8
	v_mov_b32_e32 v24, 0x40000
	v_mov_b32_e32 v25, 0
	ds_or_b64 v27, v[24:25]
	s_mov_b64 exec, -1
	v_cmp_lt_u32_e32 vcc, s36, v51
	s_mov_b64 exec, vcc
	ds_write_b32 v9, v51 offset:4864
	v_bfe_u32 v27, v51, 4, 4
	v_add_u32_e32 v6, 1, v6
	v_lshlrev_b32_e64 v28, v27, s35
	v_or_b32_e32 v7, v7, v28
	v_lshl_add_u32 v27, v27, 9, v8
	v_mov_b32_e32 v24, 0x80000
	v_mov_b32_e32 v25, 0
	ds_or_b64 v27, v[24:25]
	s_mov_b64 exec, -1
	s_cmp_le_u32 s14, 20
	s_cbranch_scc1 .Lro_built
	v_cmp_lt_u32_e32 vcc, s36, v52
	s_mov_b64 exec, vcc
	ds_write_b32 v9, v52 offset:5120
	v_bfe_u32 v27, v52, 4, 4
	v_add_u32_e32 v6, 1, v6
	v_lshlrev_b32_e64 v28, v27, s35
	v_or_b32_e32 v7, v7, v28
	v_lshl_add_u32 v27, v27, 9, v8
	v_mov_b32_e32 v24, 0x100000
	v_mov_b32_e32 v25, 0
	ds_or_b64 v27, v[24:25]
	s_mov_b64 exec, -1
	v_cmp_lt_u32_e32 vcc, s36, v53
	s_mov_b64 exec, vcc
	ds_write_b32 v9, v53 offset:5376
	v_bfe_u32 v27, v53, 4, 4
	v_add_u32_e32 v6, 1, v6
	v_lshlrev_b32_e64 v28, v27, s35
	v_or_b32_e32 v7, v7, v28
	v_lshl_add_u32 v27, v27, 9, v8
	v_mov_b32_e32 v24, 0x200000
	v_mov_b32_e32 v25, 0
	ds_or_b64 v27, v[24:25]
	s_mov_b64 exec, -1
	v_cmp_lt_u32_e32 vcc, s36, v54
	s_mov_b64 exec, vcc
	ds_write_b32 v9, v54 offset:5632
	v_bfe_u32 v27, v54, 4, 4
	v_add_u32_e32 v6, 1, v6
	v_lshlrev_b32_e64 v28, v27, s35
	v_or_b32_e32 v7, v7, v28
	v_lshl_add_u32 v27, v27, 9, v8
	v_mov_b32_e32 v24, 0x400000
	v_mov_b32_e32 v25, 0
	ds_or_b64 v27, v[24:25]
	s_mov_b64 exec, -1
	v_cmp_lt_u32_e32 vcc, s36, v55
	s_mov_b64 exec, vcc
	ds_write_b32 v9, v55 offset:5888
	v_bfe_u32 v27, v55, 4, 4
	v_add_u32_e32 v6, 1, v6
	v_lshlrev_b32_e64 v28, v27, s35
	v_or_b32_e32 v7, v7, v28
	v_lshl_add_u32 v27, v27, 9, v8
	v_mov_b32_e32 v24, 0x800000
	v_mov_b32_e32 v25, 0
	ds_or_b64 v27, v[24:25]
	s_mov_b64 exec, -1
	s_cmp_le_u32 s14, 24
	s_cbranch_scc1 .Lro_built
	v_cmp_lt_u32_e32 vcc, s36, v56
	s_mov_b64 exec, vcc
	ds_write_b32 v9, v56 offset:6144
	v_bfe_u32 v27, v56, 4, 4
	v_add_u32_e32 v6, 1, v6
	v_lshlrev_b32_e64 v28, v27, s35
	v_or_b32_e32 v7, v7, v28
	v_lshl_add_u32 v27, v27, 9, v8
	v_mov_b32_e32 v24, 0x1000000
	v_mov_b32_e32 v25, 0
	ds_or_b64 v27, v[24:25]
	s_mov_b64 exec, -1
	v_cmp_lt_u32_e32 vcc, s36, v57
	s_mov_b64 exec, vcc
	ds_write_b32 v9, v57 offset:6400
	v_bfe_u32 v27, v57, 4, 4
	v_add_u32_e32 v6, 1, v6
	v_lshlrev_b32_e64 v28, v27, s35
	v_or_b32_e32 v7, v7, v28
	v_lshl_add_u32 v27, v27, 9, v8
	v_mov_b32_e32 v24, 0x2000000
	v_mov_b32_e32 v25, 0
	ds_or_b64 v27, v[24:25]
	s_mov_b64 exec, -1
	v_cmp_lt_u32_e32 vcc, s36, v58
	s_mov_b64 exec, vcc
	ds_write_b32 v9, v58 offset:6656
	v_bfe_u32 v27, v58, 4, 4
	v_add_u32_e32 v6, 1, v6
	v_lshlrev_b32_e64 v28, v27, s35
	v_or_b32_e32 v7, v7, v28
	v_lshl_add_u32 v27, v27, 9, v8
	v_mov_b32_e32 v24, 0x4000000
	v_mov_b32_e32 v25, 0
	ds_or_b64 v27, v[24:25]
	s_mov_b64 exec, -1
	v_cmp_lt_u32_e32 vcc, s36, v59
	s_mov_b64 exec, vcc
	ds_write_b32 v9, v59 offset:6912
	v_bfe_u32 v27, v59, 4, 4
	v_add_u32_e32 v6, 1, v6
	v_lshlrev_b32_e64 v28, v27, s35
	v_or_b32_e32 v7, v7, v28
	v_lshl_add_u32 v27, v27, 9, v8
	v_mov_b32_e32 v24, 0x8000000
	v_mov_b32_e32 v25, 0
	ds_or_b64 v27, v[24:25]
	s_mov_b64 exec, -1
	s_cmp_le_u32 s14, 28
	s_cbranch_scc1 .Lro_built
	v_cmp_lt_u32_e32 vcc, s36, v60
	s_mov_b64 exec, vcc
	ds_write_b32 v9, v60 offset:7168
	v_bfe_u32 v27, v60, 4, 4
	v_add_u32_e32 v6, 1, v6
	v_lshlrev_b32_e64 v28, v27, s35
	v_or_b32_e32 v7, v7, v28
	v_lshl_add_u32 v27, v27, 9, v8
	v_mov_b32_e32 v24, 0x10000000
	v_mov_b32_e32 v25, 0
	ds_or_b64 v27, v[24:25]
	s_mov_b64 exec, -1
	v_cmp_lt_u32_e32 vcc, s36, v61
	s_mov_b64 exec, vcc
	ds_write_b32 v9, v61 offset:7424
	v_bfe_u32 v27, v61, 4, 4
	v_add_u32_e32 v6, 1, v6
	v_lshlrev_b32_e64 v28, v27, s35
	v_or_b32_e32 v7, v7, v28
	v_lshl_add_u32 v27, v27, 9, v8
	v_mov_b32_e32 v24, 0x20000000
	v_mov_b32_e32 v25, 0
	ds_or_b64 v27, v[24:25]
	s_mov_b64 exec, -1
	v_cmp_lt_u32_e32 vcc, s36, v62
	s_mov_b64 exec, vcc
	ds_write_b32 v9, v62 offset:7680
	v_bfe_u32 v27, v62, 4, 4
	v_add_u32_e32 v6, 1, v6
	v_lshlrev_b32_e64 v28, v27, s35
	v_or_b32_e32 v7, v7, v28
	v_lshl_add_u32 v27, v27, 9, v8
	v_mov_b32_e32 v24, 0x40000000
	v_mov_b32_e32 v25, 0
	ds_or_b64 v27, v[24:25]
	s_mov_b64 exec, -1
	v_cmp_lt_u32_e32 vcc, s36, v63
	s_mov_b64 exec, vcc
	ds_write_b32 v9, v63 offset:7936
	v_bfe_u32 v27, v63, 4, 4
	v_add_u32_e32 v6, 1, v6
	v_lshlrev_b32_e64 v28, v27, s35
	v_or_b32_e32 v7, v7, v28
	v_lshl_add_u32 v27, v27, 9, v8
	v_mov_b32_e32 v24, 0x80000000
	v_mov_b32_e32 v25, 0
	ds_or_b64 v27, v[24:25]
	s_mov_b64 exec, -1
	s_cmp_le_u32 s14, 32
	s_cbranch_scc1 .Lro_built
	v_cmp_lt_u32_e32 vcc, s36, v64
	s_mov_b64 exec, vcc
	ds_write_b32 v9, v64 offset:8192
	v_bfe_u32 v27, v64, 4, 4
	v_add_u32_e32 v6, 1, v6
	v_lshlrev_b32_e64 v28, v27, s35
	v_or_b32_e32 v7, v7, v28
	v_lshl_add_u32 v27, v27, 9, v8
	v_mov_b32_e32 v24, 0
	v_mov_b32_e32 v25, 1
	ds_or_b64 v27, v[24:25]
	s_mov_b64 exec, -1
	v_cmp_lt_u32_e32 vcc, s36, v65
	s_mov_b64 exec, vcc
	ds_write_b32 v9, v65 offset:8448
	v_bfe_u32 v27, v65, 4, 4
	v_add_u32_e32 v6, 1, v6
	v_lshlrev_b32_e64 v28, v27, s35
	v_or_b32_e32 v7, v7, v28
	v_lshl_add_u32 v27, v27, 9, v8
	v_mov_b32_e32 v24, 0
	v_mov_b32_e32 v25, 2
	ds_or_b64 v27, v[24:25]
	s_mov_b64 exec, -1
	v_cmp_lt_u32_e32 vcc, s36, v66
	s_mov_b64 exec, vcc
	ds_write_b32 v9, v66 offset:8704
	v_bfe_u32 v27, v66, 4, 4
	v_add_u32_e32 v6, 1, v6
	v_lshlrev_b32_e64 v28, v27, s35
	v_or_b32_e32 v7, v7, v28
	v_lshl_add_u32 v27, v27, 9, v8
	v_mov_b32_e32 v24, 0
	v_mov_b32_e32 v25, 4
	ds_or_b64 v27, v[24:25]
	s_mov_b64 exec, -1
	v_cmp_lt_u32_e32 vcc, s36, v67
	s_mov_b64 exec, vcc
	ds_write_b32 v9, v67 offset:8960
	v_bfe_u32 v27, v67, 4, 4
	v_add_u32_e32 v6, 1, v6
	v_lshlrev_b32_e64 v28, v27, s35
	v_or_b32_e32 v7, v7, v28
	v_lshl_add_u32 v27, v27, 9, v8
	v_mov_b32_e32 v24, 0
	v_mov_b32_e32 v25, 8
	ds_or_b64 v27, v[24:25]
	s_mov_b64 exec, -1
	s_cmp_le_u32 s14, 36
	s_cbranch_scc1 .Lro_built
	v_cmp_lt_u32_e32 vcc, s36, v68
	s_mov_b64 exec, vcc
	ds_write_b32 v9, v68 offset:9216
	v_bfe_u32 v27, v68, 4, 4
	v_add_u32_e32 v6, 1, v6
	v_lshlrev_b32_e64 v28, v27, s35
	v_or_b32_e32 v7, v7, v28
	v_lshl_add_u32 v27, v27, 9, v8
	v_mov_b32_e32 v24, 0
	v_mov_b32_e32 v25, 16
	ds_or_b64 v27, v[24:25]
	s_mov_b64 exec, -1
	v_cmp_lt_u32_e32 vcc, s36, v69
	s_mov_b64 exec, vcc
	ds_write_b32 v9, v69 offset:9472
	v_bfe_u32 v27, v69, 4, 4
	v_add_u32_e32 v6, 1, v6
	v_lshlrev_b32_e64 v28, v27, s35
	v_or_b32_e32 v7, v7, v28
	v_lshl_add_u32 v27, v27, 9, v8
	v_mov_b32_e32 v24, 0
	v_mov_b32_e32 v25, 32
	ds_or_b64 v27, v[24:25]
	s_mov_b64 exec, -1
	v_cmp_lt_u32_e32 vcc, s36, v70
	s_mov_b64 exec, vcc
	ds_write_b32 v9, v70 offset:9728
	v_bfe_u32 v27, v70, 4, 4
	v_add_u32_e32 v6, 1, v6
	v_lshlrev_b32_e64 v28, v27, s35
	v_or_b32_e32 v7, v7, v28
	v_lshl_add_u32 v27, v27, 9, v8
	v_mov_b32_e32 v24, 0
	v_mov_b32_e32 v25, 64
	ds_or_b64 v27, v[24:25]
	s_mov_b64 exec, -1
	v_cmp_lt_u32_e32 vcc, s36, v71
	s_mov_b64 exec, vcc
	ds_write_b32 v9, v71 offset:9984
	v_bfe_u32 v27, v71, 4, 4
	v_add_u32_e32 v6, 1, v6
	v_lshlrev_b32_e64 v28, v27, s35
	v_or_b32_e32 v7, v7, v28
	v_lshl_add_u32 v27, v27, 9, v8
	v_mov_b32_e32 v24, 0
	v_mov_b32_e32 v25, 0x80
	ds_or_b64 v27, v[24:25]
	s_mov_b64 exec, -1
	s_cmp_le_u32 s14, 40
	s_cbranch_scc1 .Lro_built
	v_cmp_lt_u32_e32 vcc, s36, v72
	s_mov_b64 exec, vcc
	ds_write_b32 v9, v72 offset:10240
	v_bfe_u32 v27, v72, 4, 4
	v_add_u32_e32 v6, 1, v6
	v_lshlrev_b32_e64 v28, v27, s35
	v_or_b32_e32 v7, v7, v28
	v_lshl_add_u32 v27, v27, 9, v8
	v_mov_b32_e32 v24, 0
	v_mov_b32_e32 v25, 0x100
	ds_or_b64 v27, v[24:25]
	s_mov_b64 exec, -1
	v_cmp_lt_u32_e32 vcc, s36, v73
	s_mov_b64 exec, vcc
	ds_write_b32 v9, v73 offset:10496
	v_bfe_u32 v27, v73, 4, 4
	v_add_u32_e32 v6, 1, v6
	v_lshlrev_b32_e64 v28, v27, s35
	v_or_b32_e32 v7, v7, v28
	v_lshl_add_u32 v27, v27, 9, v8
	v_mov_b32_e32 v24, 0
	v_mov_b32_e32 v25, 0x200
	ds_or_b64 v27, v[24:25]
	s_mov_b64 exec, -1
	v_cmp_lt_u32_e32 vcc, s36, v74
	s_mov_b64 exec, vcc
	ds_write_b32 v9, v74 offset:10752
	v_bfe_u32 v27, v74, 4, 4
	v_add_u32_e32 v6, 1, v6
	v_lshlrev_b32_e64 v28, v27, s35
	v_or_b32_e32 v7, v7, v28
	v_lshl_add_u32 v27, v27, 9, v8
	v_mov_b32_e32 v24, 0
	v_mov_b32_e32 v25, 0x400
	ds_or_b64 v27, v[24:25]
	s_mov_b64 exec, -1
	v_cmp_lt_u32_e32 vcc, s36, v75
	s_mov_b64 exec, vcc
	ds_write_b32 v9, v75 offset:11008
	v_bfe_u32 v27, v75, 4, 4
	v_add_u32_e32 v6, 1, v6
	v_lshlrev_b32_e64 v28, v27, s35
	v_or_b32_e32 v7, v7, v28
	v_lshl_add_u32 v27, v27, 9, v8
	v_mov_b32_e32 v24, 0
	v_mov_b32_e32 v25, 0x800
	ds_or_b64 v27, v[24:25]
	s_mov_b64 exec, -1
	s_cmp_le_u32 s14, 44
	s_cbranch_scc1 .Lro_built
	v_cmp_lt_u32_e32 vcc, s36, v76
	s_mov_b64 exec, vcc
	ds_write_b32 v9, v76 offset:11264
	v_bfe_u32 v27, v76, 4, 4
	v_add_u32_e32 v6, 1, v6
	v_lshlrev_b32_e64 v28, v27, s35
	v_or_b32_e32 v7, v7, v28
	v_lshl_add_u32 v27, v27, 9, v8
	v_mov_b32_e32 v24, 0
	v_mov_b32_e32 v25, 0x1000
	ds_or_b64 v27, v[24:25]
	s_mov_b64 exec, -1
	v_cmp_lt_u32_e32 vcc, s36, v77
	s_mov_b64 exec, vcc
	ds_write_b32 v9, v77 offset:11520
	v_bfe_u32 v27, v77, 4, 4
	v_add_u32_e32 v6, 1, v6
	v_lshlrev_b32_e64 v28, v27, s35
	v_or_b32_e32 v7, v7, v28
	v_lshl_add_u32 v27, v27, 9, v8
	v_mov_b32_e32 v24, 0
	v_mov_b32_e32 v25, 0x2000
	ds_or_b64 v27, v[24:25]
	s_mov_b64 exec, -1
	v_cmp_lt_u32_e32 vcc, s36, v78
	s_mov_b64 exec, vcc
	ds_write_b32 v9, v78 offset:11776
	v_bfe_u32 v27, v78, 4, 4
	v_add_u32_e32 v6, 1, v6
	v_lshlrev_b32_e64 v28, v27, s35
	v_or_b32_e32 v7, v7, v28
	v_lshl_add_u32 v27, v27, 9, v8
	v_mov_b32_e32 v24, 0
	v_mov_b32_e32 v25, 0x4000
	ds_or_b64 v27, v[24:25]
	s_mov_b64 exec, -1
	v_cmp_lt_u32_e32 vcc, s36, v79
	s_mov_b64 exec, vcc
	ds_write_b32 v9, v79 offset:12032
	v_bfe_u32 v27, v79, 4, 4
	v_add_u32_e32 v6, 1, v6
	v_lshlrev_b32_e64 v28, v27, s35
	v_or_b32_e32 v7, v7, v28
	v_lshl_add_u32 v27, v27, 9, v8
	v_mov_b32_e32 v24, 0
	v_mov_b32_e32 v25, 0x8000
	ds_or_b64 v27, v[24:25]
	s_mov_b64 exec, -1
	s_cmp_le_u32 s14, 48
	s_cbranch_scc1 .Lro_built
	v_cmp_lt_u32_e32 vcc, s36, v80
	s_mov_b64 exec, vcc
	ds_write_b32 v9, v80 offset:12288
	v_bfe_u32 v27, v80, 4, 4
	v_add_u32_e32 v6, 1, v6
	v_lshlrev_b32_e64 v28, v27, s35
	v_or_b32_e32 v7, v7, v28
	v_lshl_add_u32 v27, v27, 9, v8
	v_mov_b32_e32 v24, 0
	v_mov_b32_e32 v25, 0x10000
	ds_or_b64 v27, v[24:25]
	s_mov_b64 exec, -1
	v_cmp_lt_u32_e32 vcc, s36, v81
	s_mov_b64 exec, vcc
	ds_write_b32 v9, v81 offset:12544
	v_bfe_u32 v27, v81, 4, 4
	v_add_u32_e32 v6, 1, v6
	v_lshlrev_b32_e64 v28, v27, s35
	v_or_b32_e32 v7, v7, v28
	v_lshl_add_u32 v27, v27, 9, v8
	v_mov_b32_e32 v24, 0
	v_mov_b32_e32 v25, 0x20000
	ds_or_b64 v27, v[24:25]
	s_mov_b64 exec, -1
	v_cmp_lt_u32_e32 vcc, s36, v82
	s_mov_b64 exec, vcc
	ds_write_b32 v9, v82 offset:12800
	v_bfe_u32 v27, v82, 4, 4
	v_add_u32_e32 v6, 1, v6
	v_lshlrev_b32_e64 v28, v27, s35
	v_or_b32_e32 v7, v7, v28
	v_lshl_add_u32 v27, v27, 9, v8
	v_mov_b32_e32 v24, 0
	v_mov_b32_e32 v25, 0x40000
	ds_or_b64 v27, v[24:25]
	s_mov_b64 exec, -1
	v_cmp_lt_u32_e32 vcc, s36, v83
	s_mov_b64 exec, vcc
	ds_write_b32 v9, v83 offset:13056
	v_bfe_u32 v27, v83, 4, 4
	v_add_u32_e32 v6, 1, v6
	v_lshlrev_b32_e64 v28, v27, s35
	v_or_b32_e32 v7, v7, v28
	v_lshl_add_u32 v27, v27, 9, v8
	v_mov_b32_e32 v24, 0
	v_mov_b32_e32 v25, 0x80000
	ds_or_b64 v27, v[24:25]
	s_mov_b64 exec, -1
	s_cmp_le_u32 s14, 52
	s_cbranch_scc1 .Lro_built
	v_cmp_lt_u32_e32 vcc, s36, v84
	s_mov_b64 exec, vcc
	ds_write_b32 v9, v84 offset:13312
	v_bfe_u32 v27, v84, 4, 4
	v_add_u32_e32 v6, 1, v6
	v_lshlrev_b32_e64 v28, v27, s35
	v_or_b32_e32 v7, v7, v28
	v_lshl_add_u32 v27, v27, 9, v8
	v_mov_b32_e32 v24, 0
	v_mov_b32_e32 v25, 0x100000
	ds_or_b64 v27, v[24:25]
	s_mov_b64 exec, -1
	v_cmp_lt_u32_e32 vcc, s36, v85
	s_mov_b64 exec, vcc
	ds_write_b32 v9, v85 offset:13568
	v_bfe_u32 v27, v85, 4, 4
	v_add_u32_e32 v6, 1, v6
	v_lshlrev_b32_e64 v28, v27, s35
	v_or_b32_e32 v7, v7, v28
	v_lshl_add_u32 v27, v27, 9, v8
	v_mov_b32_e32 v24, 0
	v_mov_b32_e32 v25, 0x200000
	ds_or_b64 v27, v[24:25]
	s_mov_b64 exec, -1
	v_cmp_lt_u32_e32 vcc, s36, v86
	s_mov_b64 exec, vcc
	ds_write_b32 v9, v86 offset:13824
	v_bfe_u32 v27, v86, 4, 4
	v_add_u32_e32 v6, 1, v6
	v_lshlrev_b32_e64 v28, v27, s35
	v_or_b32_e32 v7, v7, v28
	v_lshl_add_u32 v27, v27, 9, v8
	v_mov_b32_e32 v24, 0
	v_mov_b32_e32 v25, 0x400000
	ds_or_b64 v27, v[24:25]
	s_mov_b64 exec, -1
	v_cmp_lt_u32_e32 vcc, s36, v87
	s_mov_b64 exec, vcc
	ds_write_b32 v9, v87 offset:14080
	v_bfe_u32 v27, v87, 4, 4
	v_add_u32_e32 v6, 1, v6
	v_lshlrev_b32_e64 v28, v27, s35
	v_or_b32_e32 v7, v7, v28
	v_lshl_add_u32 v27, v27, 9, v8
	v_mov_b32_e32 v24, 0
	v_mov_b32_e32 v25, 0x800000
	ds_or_b64 v27, v[24:25]
	s_mov_b64 exec, -1
	s_cmp_le_u32 s14, 56
	s_cbranch_scc1 .Lro_built
	v_cmp_lt_u32_e32 vcc, s36, v88
	s_mov_b64 exec, vcc
	ds_write_b32 v9, v88 offset:14336
	v_bfe_u32 v27, v88, 4, 4
	v_add_u32_e32 v6, 1, v6
	v_lshlrev_b32_e64 v28, v27, s35
	v_or_b32_e32 v7, v7, v28
	v_lshl_add_u32 v27, v27, 9, v8
	v_mov_b32_e32 v24, 0
	v_mov_b32_e32 v25, 0x1000000
	ds_or_b64 v27, v[24:25]
	s_mov_b64 exec, -1
	v_cmp_lt_u32_e32 vcc, s36, v89
	s_mov_b64 exec, vcc
	ds_write_b32 v9, v89 offset:14592
	v_bfe_u32 v27, v89, 4, 4
	v_add_u32_e32 v6, 1, v6
	v_lshlrev_b32_e64 v28, v27, s35
	v_or_b32_e32 v7, v7, v28
	v_lshl_add_u32 v27, v27, 9, v8
	v_mov_b32_e32 v24, 0
	v_mov_b32_e32 v25, 0x2000000
	ds_or_b64 v27, v[24:25]
	s_mov_b64 exec, -1
	v_cmp_lt_u32_e32 vcc, s36, v90
	s_mov_b64 exec, vcc
	ds_write_b32 v9, v90 offset:14848
	v_bfe_u32 v27, v90, 4, 4
	v_add_u32_e32 v6, 1, v6
	v_lshlrev_b32_e64 v28, v27, s35
	v_or_b32_e32 v7, v7, v28
	v_lshl_add_u32 v27, v27, 9, v8
	v_mov_b32_e32 v24, 0
	v_mov_b32_e32 v25, 0x4000000
	ds_or_b64 v27, v[24:25]
	s_mov_b64 exec, -1
	v_cmp_lt_u32_e32 vcc, s36, v91
	s_mov_b64 exec, vcc
	ds_write_b32 v9, v91 offset:15104
	v_bfe_u32 v27, v91, 4, 4
	v_add_u32_e32 v6, 1, v6
	v_lshlrev_b32_e64 v28, v27, s35
	v_or_b32_e32 v7, v7, v28
	v_lshl_add_u32 v27, v27, 9, v8
	v_mov_b32_e32 v24, 0
	v_mov_b32_e32 v25, 0x8000000
	ds_or_b64 v27, v[24:25]
	s_mov_b64 exec, -1
	s_cmp_le_u32 s14, 60
	s_cbranch_scc1 .Lro_built
	v_cmp_lt_u32_e32 vcc, s36, v92
	s_mov_b64 exec, vcc
	ds_write_b32 v9, v92 offset:15360
	v_bfe_u32 v27, v92, 4, 4
	v_add_u32_e32 v6, 1, v6
	v_lshlrev_b32_e64 v28, v27, s35
	v_or_b32_e32 v7, v7, v28
	v_lshl_add_u32 v27, v27, 9, v8
	v_mov_b32_e32 v24, 0
	v_mov_b32_e32 v25, 0x10000000
	ds_or_b64 v27, v[24:25]
	s_mov_b64 exec, -1
	v_cmp_lt_u32_e32 vcc, s36, v93
	s_mov_b64 exec, vcc
	ds_write_b32 v9, v93 offset:15616
	v_bfe_u32 v27, v93, 4, 4
	v_add_u32_e32 v6, 1, v6
	v_lshlrev_b32_e64 v28, v27, s35
	v_or_b32_e32 v7, v7, v28
	v_lshl_add_u32 v27, v27, 9, v8
	v_mov_b32_e32 v24, 0
	v_mov_b32_e32 v25, 0x20000000
	ds_or_b64 v27, v[24:25]
	s_mov_b64 exec, -1
	v_cmp_lt_u32_e32 vcc, s36, v94
	s_mov_b64 exec, vcc
	ds_write_b32 v9, v94 offset:15872
	v_bfe_u32 v27, v94, 4, 4
	v_add_u32_e32 v6, 1, v6
	v_lshlrev_b32_e64 v28, v27, s35
	v_or_b32_e32 v7, v7, v28
	v_lshl_add_u32 v27, v27, 9, v8
	v_mov_b32_e32 v24, 0
	v_mov_b32_e32 v25, 0x40000000
	ds_or_b64 v27, v[24:25]
	s_mov_b64 exec, -1
	v_cmp_lt_u32_e32 vcc, s36, v95
	s_mov_b64 exec, vcc
	ds_write_b32 v9, v95 offset:16128
	v_bfe_u32 v27, v95, 4, 4
	v_add_u32_e32 v6, 1, v6
	v_lshlrev_b32_e64 v28, v27, s35
	v_or_b32_e32 v7, v7, v28
	v_lshl_add_u32 v27, v27, 9, v8
	v_mov_b32_e32 v24, 0
	v_mov_b32_e32 v25, 0x80000000
	ds_or_b64 v27, v[24:25]
	s_mov_b64 exec, -1
.Lro_built:
	s_mov_b64 exec, -1
	s_mov_b32 s18, 0
	s_waitcnt lgkmcnt(0)
.Lro_round:
	s_sub_u32 s34, s14, s18
	s_mul_i32 s32, s18, 7
	s_and_b32 s32, s32, 15
	s_mul_i32 s33, s18, 5
	v_add_u32_e32 v22, s33, v2
	v_and_b32_e32 v22, 15, v22
	v_cmp_gt_u32_e64 s[24:25], s34, v6
	v_cmp_eq_u32_e32 vcc, s32, v2
	v_mov_b32_e32 v12, 0
	s_mov_b32 s19, 16
.Lro_ripple:
	s_nop 1
	v_cndmask_b32_dpp v13, v12, v11, vcc row_ror:1 row_mask:0xf bank_mask:0xf
	v_bfi_b32 v14, v13, 0, v7
	v_not_b32_e32 v15, v13
	v_cmp_ne_u32_e64 s[26:27], 0, v14
	v_cndmask_b32_e64 v16, v7, v15, s[24:25]
	s_nop 0
	v_cndmask_b32_e64 v17, v16, v14, s[26:27]
	v_lshrrev_b32_e32 v18, v22, v17
	v_ffbl_b32_e32 v19, v18
	v_add_u32_e32 v20, v19, v22
	v_and_b32_e32 v20, 15, v20
	v_lshlrev_b32_e64 v21, v20, s35
	v_or_b32_e32 v12, v13, v21
	s_sub_u32 s19, s19, 1
	s_cmp_lg_u32 s19, 0
	s_cbranch_scc1 .Lro_ripple
	s_orn2_b64 s[28:29], s[26:27], s[24:25]
	v_lshlrev_b32_e32 v29, 4, v20
	s_and_saveexec_b64 s[22:23], s[28:29]
	s_cbranch_execz .Lro_nopop
	v_lshl_add_u32 v30, v20, 9, v8
	ds_read_b64 v[24:25], v30
	s_waitcnt lgkmcnt(0)
	v_ffbl_b32_e32 v26, v24
	v_ffbl_b32_e32 v27, v25
	v_add_u32_e32 v27, 32, v27
	v_min_u32_e32 v28, v26, v27
	v_lshlrev_b64 v[26:27], v28, 1
	v_bfi_b32 v24, v26, 0, v24
	v_bfi_b32 v25, v27, 0, v25
	ds_write_b64 v30, v[24:25]
	v_lshl_add_u32 v26, v28, 8, v9
	ds_read_b32 v29, v26
	v_or_b32_e32 v24, v24, v25
	v_cmp_eq_u32_e32 vcc, 0, v24
	v_bfi_b32 v27, v21, 0, v7
	s_nop 1
	v_cndmask_b32_e32 v7, v7, v27, vcc
	v_subrev_u32_e32 v6, 1, v6
	s_waitcnt lgkmcnt(0)
.Lro_nopop:
	s_or_b64 exec, exec, s[22:23]
	s_lshr_b32 s20, s18, 2
	s_lshl_b32 s20, s20, 10
	s_and_b32 s21, s18, 3
	s_lshl_b32 s21, s21, 2
	s_add_u32 s20, s20, s21
	s_add_u32 s30, s16, s20
	s_addc_u32 s31, s17, 0
	global_store_dword v10, v29, s[30:31]
	s_add_u32 s18, s18, 1
	s_cmp_lt_u32 s18, s14
	s_cbranch_scc1 .Lro_round

	.amdhsa_kernel _Z7k_conv1PKfS0_S0_Pf
		.amdhsa_group_segment_fixed_size 32768
		.amdhsa_private_segment_fixed_size 0
		.amdhsa_kernarg_size 32
		.amdhsa_user_sgpr_count 2
		.amdhsa_user_sgpr_dispatch_ptr 0
		.amdhsa_user_sgpr_queue_ptr 0
		.amdhsa_user_sgpr_kernarg_segment_ptr 1
		.amdhsa_user_sgpr_dispatch_id 0
		.amdhsa_user_sgpr_kernarg_preload_length 0
		.amdhsa_user_sgpr_kernarg_preload_offset 0
		.amdhsa_user_sgpr_private_segment_size 0
		.amdhsa_uses_dynamic_stack 0
		.amdhsa_enable_private_segment 0
		.amdhsa_system_sgpr_workgroup_id_x 1
		.amdhsa_system_sgpr_workgroup_id_y 0
		.amdhsa_system_sgpr_workgroup_id_z 0
		.amdhsa_system_sgpr_workgroup_info 0
		.amdhsa_system_vgpr_workitem_id 0
		.amdhsa_next_free_vgpr 107
		.amdhsa_next_free_sgpr 40
		.amdhsa_accum_offset 108
		.amdhsa_reserve_vcc 1
		.amdhsa_float_round_mode_32 0
		.amdhsa_float_round_mode_16_64 0
		.amdhsa_float_denorm_mode_32 3
		.amdhsa_float_denorm_mode_16_64 3
		.amdhsa_dx10_clamp 1
		.amdhsa_ieee_mode 1
		.amdhsa_fp16_overflow 0
		.amdhsa_tg_split 0
		.amdhsa_exception_fp_ieee_invalid_op 0
		.amdhsa_exception_fp_denorm_src 0
		.amdhsa_exception_fp_ieee_div_zero 0
		.amdhsa_exception_fp_ieee_overflow 0
		.amdhsa_exception_fp_ieee_underflow 0
		.amdhsa_exception_fp_ieee_inexact 0
		.amdhsa_exception_int_div_zero 0
	.end_amdhsa_kernel

amdhsa.kernels:
  - .agpr_count:     0
    .args:
      - .actual_access:  read_only
        .address_space:  global
        .offset:         0
        .size:           8
        .value_kind:     global_buffer
      - .actual_access:  read_only
        .address_space:  global
        .offset:         8
        .size:           8
        .value_kind:     global_buffer
      - .actual_access:  write_only
        .address_space:  global
        .offset:         16
        .size:           8
        .value_kind:     global_buffer
      - .actual_access:  write_only
        .address_space:  global
        .offset:         24
        .size:           8
        .value_kind:     global_buffer
      - .actual_access:  write_only
        .address_space:  global
        .offset:         32
        .size:           8
        .value_kind:     global_buffer
      - .actual_access:  read_only
        .address_space:  global
        .offset:         40
        .size:           8
        .value_kind:     global_buffer
    .group_segment_fixed_size: 1024
    .kernarg_segment_align: 8
    .kernarg_segment_size: 48
    .language:       OpenCL C
    .language_version:
      - 2
      - 0
    .max_flat_workgroup_size: 1024
    .name:           _Z7k_sort2PKiPKfPiS3_S3_Pf
    .private_segment_fixed_size: 0
    .sgpr_count:     18
    .sgpr_spill_count: 0
    .symbol:         _Z7k_sort2PKiPKfPiS3_S3_Pf.kd
    .uniform_work_group_size: 1
    .uses_dynamic_stack: false
    .vgpr_count:     21
    .vgpr_spill_count: 0
    .wavefront_size: 64
  - .agpr_count:     0
    .args:
      - .actual_access:  read_only
        .address_space:  global
        .offset:         0
        .size:           8
        .value_kind:     global_buffer
      - .actual_access:  read_only
        .address_space:  global
        .offset:         8
        .size:           8
        .value_kind:     global_buffer
      - .actual_access:  read_only
        .address_space:  global
        .offset:         16
        .size:           8
        .value_kind:     global_buffer
      - .actual_access:  read_only
        .address_space:  global
        .offset:         24
        .size:           8
        .value_kind:     global_buffer
      - .actual_access:  read_only
        .address_space:  global
        .offset:         32
        .size:           8
        .value_kind:     global_buffer
      - .actual_access:  read_only
        .address_space:  global
        .offset:         40
        .size:           8
        .value_kind:     global_buffer
      - .address_space:  global
        .offset:         48
        .size:           8
        .value_kind:     global_buffer
      - .address_space:  global
        .offset:         56
        .size:           8
        .value_kind:     global_buffer
      - .offset:         64
        .size:           4
        .value_kind:     by_value
      - .offset:         68
        .size:           4
        .value_kind:     by_value
    .group_segment_fixed_size: 0
    .kernarg_segment_align: 8
    .kernarg_segment_size: 72
    .language:       OpenCL C
    .language_version:
      - 2
      - 0
    .max_flat_workgroup_size: 512
    .name:           _Z7k_spmm1PKiS0_PKfPK15HIP_vector_typeIjLj2EES0_S2_S2_Pfff
    .private_segment_fixed_size: 0
    .sgpr_count:     26
    .sgpr_spill_count: 0
    .symbol:         _Z7k_spmm1PKiS0_PKfPK15HIP_vector_typeIjLj2EES0_S2_S2_Pfff.kd
    .uniform_work_group_size: 1
    .uses_dynamic_stack: false
    .vgpr_count:     41
    .vgpr_spill_count: 0
    .wavefront_size: 64
  - .agpr_count:     0
    .args:
      - .address_space:  global
        .offset:         0
        .size:           8
        .value_kind:     global_buffer
      - .actual_access:  read_only
        .address_space:  global
        .offset:         8
        .size:           8
        .value_kind:     global_buffer
      - .actual_access:  read_only
        .address_space:  global
        .offset:         16
        .size:           8
        .value_kind:     global_buffer
      - .actual_access:  write_only
        .address_space:  global
        .offset:         24
        .size:           8
        .value_kind:     global_buffer
    .group_segment_fixed_size: 32768
    .kernarg_segment_align: 8
    .kernarg_segment_size: 32
    .language:       OpenCL C
    .language_version:
      - 2
      - 0
    .max_flat_workgroup_size: 512
    .name:           _Z7k_conv1PKfS0_S0_Pf
    .private_segment_fixed_size: 0
    .sgpr_count:     46
    .sgpr_spill_count: 0
    .symbol:         _Z7k_conv1PKfS0_S0_Pf.kd
    .uniform_work_group_size: 1
    .uses_dynamic_stack: false
    .vgpr_count:     107
    .vgpr_spill_count: 0
    .wavefront_size: 64
  - .agpr_count:     0
    .args:
      - .actual_access:  read_only
        .address_space:  global
        .offset:         0
        .size:           8
        .value_kind:     global_buffer
      - .actual_access:  read_only
        .address_space:  global
        .offset:         8
        .size:           8
        .value_kind:     global_buffer
      - .actual_access:  read_only
        .address_space:  global
        .offset:         16
        .size:           8
        .value_kind:     global_buffer
      - .address_space:  global
        .offset:         24
        .size:           8
        .value_kind:     global_buffer
      - .actual_access:  read_only
        .address_space:  global
        .offset:         32
        .size:           8
        .value_kind:     global_buffer
      - .actual_access:  read_only
        .address_space:  global
        .offset:         40
        .size:           8
        .value_kind:     global_buffer
      - .actual_access:  write_only
        .address_space:  global
        .offset:         48
        .size:           8
        .value_kind:     global_buffer
      - .actual_access:  write_only
        .address_space:  global
        .offset:         56
        .size:           8
        .value_kind:     global_buffer
      - .actual_access:  write_only
        .address_space:  global
        .offset:         64
        .size:           8
        .value_kind:     global_buffer
    .group_segment_fixed_size: 139392
    .kernarg_segment_align: 8
    .kernarg_segment_size: 72
    .language:       OpenCL C
    .language_version:
      - 2
      - 0
    .max_flat_workgroup_size: 512
    .name:           _Z6k_rec2PKiS0_S0_PK15HIP_vector_typeIjLj4EEPKfS6_PS2_PS1_IjLj2EEPf
    .private_segment_fixed_size: 0
    .sgpr_count:     75
    .sgpr_spill_count: 0
    .symbol:         _Z6k_rec2PKiS0_S0_PK15HIP_vector_typeIjLj4EEPKfS6_PS2_PS1_IjLj2EEPf.kd
    .uniform_work_group_size: 1
    .uses_dynamic_stack: false
    .vgpr_count:     246
    .vgpr_spill_count: 0
    .wavefront_size: 64
  - .agpr_count:     0
    .args:
      - .address_space:  global
        .offset:         0
        .size:           8
        .value_kind:     global_buffer
      - .address_space:  global
        .offset:         8
        .size:           8
        .value_kind:     global_buffer
      - .actual_access:  read_only
        .address_space:  global
        .offset:         16
        .size:           8
        .value_kind:     global_buffer
      - .actual_access:  read_only
        .address_space:  global
        .offset:         24
        .size:           8
        .value_kind:     global_buffer
      - .actual_access:  read_only
        .address_space:  global
        .offset:         32
        .size:           8
        .value_kind:     global_buffer
      - .actual_access:  read_only
        .address_space:  global
        .offset:         40
        .size:           8
        .value_kind:     global_buffer
      - .actual_access:  write_only
        .address_space:  global
        .offset:         48
        .size:           8
        .value_kind:     global_buffer
      - .actual_access:  write_only
        .address_space:  global
        .offset:         56
        .size:           8
        .value_kind:     global_buffer
    .group_segment_fixed_size: 127376
    .kernarg_segment_align: 8
    .kernarg_segment_size: 64
    .language:       OpenCL C
    .language_version:
      - 2
      - 0
    .max_flat_workgroup_size: 1024
    .name:           _Z7k_gemm2PK15HIP_vector_typeIjLj4EEPKS_IjLj2EEPKfS2_S2_S7_PtS8_
    .private_segment_fixed_size: 0
    .sgpr_count:     26
    .sgpr_spill_count: 0
    .symbol:         _Z7k_gemm2PK15HIP_vector_typeIjLj4EEPKS_IjLj2EEPKfS2_S2_S7_PtS8_.kd
    .uniform_work_group_size: 1
    .uses_dynamic_stack: false
    .vgpr_count:     115
    .vgpr_spill_count: 0
    .wavefront_size: 64
  - .agpr_count:     32
    .args:
      - .address_space:  global
        .offset:         0
        .size:           8
        .value_kind:     global_buffer
      - .address_space:  global
        .offset:         8
        .size:           8
        .value_kind:     global_buffer
      - .address_space:  global
        .offset:         16
        .size:           8
        .value_kind:     global_buffer
      - .actual_access:  write_only
        .address_space:  global
        .offset:         24
        .size:           8
        .value_kind:     global_buffer
    .group_segment_fixed_size: 65536
    .kernarg_segment_align: 8
    .kernarg_segment_size: 32
    .language:       OpenCL C
    .language_version:
      - 2
      - 0
    .max_flat_workgroup_size: 256
    .name:           _Z5k_fc1PKtS0_PKfPf
    .private_segment_fixed_size: 0
    .sgpr_count:     49
    .sgpr_spill_count: 0
    .symbol:         _Z5k_fc1PKtS0_PKfPf.kd
    .uniform_work_group_size: 1
    .uses_dynamic_stack: false
    .vgpr_count:     172
    .vgpr_spill_count: 0
    .wavefront_size: 64
  - .agpr_count:     0
    .args:
      - .actual_access:  read_only
        .address_space:  global
        .offset:         0
        .size:           8
        .value_kind:     global_buffer
      - .actual_access:  read_only
        .address_space:  global
        .offset:         8
        .size:           8
        .value_kind:     global_buffer
      - .actual_access:  read_only
        .address_space:  global
        .offset:         16
        .size:           8
        .value_kind:     global_buffer
      - .actual_access:  read_only
        .address_space:  global
        .offset:         24
        .size:           8
        .value_kind:     global_buffer
      - .actual_access:  write_only
        .address_space:  global
        .offset:         32
        .size:           8
        .value_kind:     global_buffer
    .group_segment_fixed_size: 2048
    .kernarg_segment_align: 8
    .kernarg_segment_size: 40
    .language:       OpenCL C
    .language_version:
      - 2
      - 0
    .max_flat_workgroup_size: 512
    .name:           _Z5k_fc2PKfS0_S0_S0_Pf
    .private_segment_fixed_size: 0
    .sgpr_count:     18
    .sgpr_spill_count: 0
    .symbol:         _Z5k_fc2PKfS0_S0_S0_Pf.kd
    .uniform_work_group_size: 1
    .uses_dynamic_stack: false
    .vgpr_count:     96
    .vgpr_spill_count: 0
    .wavefront_size: 64
  - .agpr_count:     0
    .args:
      - .actual_access:  read_only
        .address_space:  global
        .offset:         0
        .size:           8
        .value_kind:     global_buffer
      - .actual_access:  read_only
        .address_space:  global
        .offset:         8
        .size:           8
        .value_kind:     global_buffer
      - .actual_access:  read_only
        .address_space:  global
        .offset:         16
        .size:           8
        .value_kind:     global_buffer
      - .actual_access:  read_only
        .address_space:  global
        .offset:         24
        .size:           8
        .value_kind:     global_buffer
      - .actual_access:  write_only
        .address_space:  global
        .offset:         32
        .size:           8
        .value_kind:     global_buffer
      - .actual_access:  write_only
        .address_space:  global
        .offset:         40
        .size:           8
        .value_kind:     global_buffer
      - .actual_access:  write_only
        .address_space:  global
        .offset:         48
        .size:           8
        .value_kind:     global_buffer
      - .actual_access:  write_only
        .address_space:  global
        .offset:         56
        .size:           8
        .value_kind:     global_buffer
      - .actual_access:  write_only
        .address_space:  global
        .offset:         64
        .size:           8
        .value_kind:     global_buffer
    .group_segment_fixed_size: 16640
    .kernarg_segment_align: 8
    .kernarg_segment_size: 72
    .language:       OpenCL C
    .language_version:
      - 2
      - 0
    .max_flat_workgroup_size: 256
    .name:           _Z7k_prepAPKiS0_PKfS2_PiS3_PtS4_Pf
    .private_segment_fixed_size: 0
    .sgpr_count:     20
    .sgpr_spill_count: 0
    .symbol:         _Z7k_prepAPKiS0_PKfS2_PiS3_PtS4_Pf.kd
    .uniform_work_group_size: 1
    .uses_dynamic_stack: false
    .vgpr_count:     24
    .vgpr_spill_count: 0
    .wavefront_size: 64
  - .agpr_count:     0
    .args:
      - .actual_access:  read_only
        .address_space:  global
        .offset:         0
        .size:           8
        .value_kind:     global_buffer
      - .actual_access:  read_only
        .address_space:  global
        .offset:         8
        .size:           8
        .value_kind:     global_buffer
      - .actual_access:  read_only
        .address_space:  global
        .offset:         16
        .size:           8
        .value_kind:     global_buffer
      - .actual_access:  write_only
        .address_space:  global
        .offset:         24
        .size:           8
        .value_kind:     global_buffer
      - .actual_access:  write_only
        .address_space:  global
        .offset:         32
        .size:           8
        .value_kind:     global_buffer
      - .actual_access:  read_only
        .address_space:  global
        .offset:         40
        .size:           8
        .value_kind:     global_buffer
      - .actual_access:  read_only
        .address_space:  global
        .offset:         48
        .size:           8
        .value_kind:     global_buffer
      - .actual_access:  read_only
        .address_space:  global
        .offset:         56
        .size:           8
        .value_kind:     global_buffer
      - .actual_access:  read_only
        .address_space:  global
        .offset:         64
        .size:           8
        .value_kind:     global_buffer
      - .actual_access:  read_only
        .address_space:  global
        .offset:         72
        .size:           8
        .value_kind:     global_buffer
      - .actual_access:  read_only
        .address_space:  global
        .offset:         80
        .size:           8
        .value_kind:     global_buffer
      - .actual_access:  read_only
        .address_space:  global
        .offset:         88
        .size:           8
        .value_kind:     global_buffer
      - .actual_access:  write_only
        .address_space:  global
        .offset:         96
        .size:           8
        .value_kind:     global_buffer
    .group_segment_fixed_size: 0
    .kernarg_segment_align: 8
    .kernarg_segment_size: 104
    .language:       OpenCL C
    .language_version:
      - 2
      - 0
    .max_flat_workgroup_size: 256
    .name:           _Z7k_prepBPKiS0_PKfP15HIP_vector_typeIjLj2EEPiS0_S0_S2_S0_S0_S0_S2_Pj
    .private_segment_fixed_size: 0
    .sgpr_count:     21
    .sgpr_spill_count: 0
    .symbol:         _Z7k_prepBPKiS0_PKfP15HIP_vector_typeIjLj2EEPiS0_S0_S2_S0_S0_S0_S2_Pj.kd
    .uniform_work_group_size: 1
    .uses_dynamic_stack: false
    .vgpr_count:     14
    .vgpr_spill_count: 0
    .wavefront_size: 64
